# on top of foxpipe: SWA attention compute also issues all 8 K-fragment ds_reads up front with counted lgkmcnt waits
# baseline (speedup 1.0000x reference)
; #define LAS __attribute__((address_space(3)))
; template <int D, bool MASK, bool BIAS, bool SINK, bool REV, bool O8, class BG>
; __device__ __forceinline__ void attn_unit(const Prm& P, LAS unsigned char* lds, BG& bg) {
;     ...
;         bool compute = true, need_mask = false;
;         if (MASK) {
;             compute = !(kbase > qw + 31 || kbase + 63 < qw - P.window + 1) && (!REV || need_cur != 0);
;             need_mask = (kbase + 63 > qw) || (kbase < qw + 31 - P.window + 1) || (kbase < 0);
;         }
;         if (compute) {
;             const float cinit = cq - mhat;
;             f32x16 p0, p1;
; #pragma unroll
;             for (int r = 0; r < 16; ++r) { p0[r] = cinit; p1[r] = cinit; }
;             const LAS unsigned char* ks = lds + KOFF + s * KSLOT + hi * 1024 + r32 * 16;
; #pragma unroll
;             for (int d0 = 0; d0 < NKS; ++d0) {
;                 const bf16x8 b0 = *(const LAS bf16x8*)(ks + d0 * 2048), b1 = *(const LAS bf16x8*)(ks + d0 * 2048 + 512);
;                 p0 = __builtin_amdgcn_mfma_f32_32x32x16_bf16(b0, qr[d0], p0, 0, 0, 0);
;                 p1 = __builtin_amdgcn_mfma_f32_32x32x16_bf16(b1, qr[d0], p1, 0, 0, 0);
;             }
;             if (BIAS) {
;                 const LAS float* cb = P.c + (kbase - P.cpos0) + 4 * hi;
; #pragma unroll
;                 for (int g = 0; g < 4; ++g) {
;                     const f32x4 a = *(const LAS f32x4*)(cb + 8 * g), b = *(const LAS f32x4*)(cb + 32 + 8 * g);
; #pragma unroll
;                     for (int j = 0; j < 4; ++j) { p0[4 * g + j] -= a[j]; p1[4 * g + j] -= b[j]; }
;                 }
.LBB0_603:
	s_cmp_le_i32 s62, s68
	s_cselect_b64 s[80:81], -1, 0
	s_or_b32 s6, s62, 63
	s_cmp_gt_i32 s6, s69
	s_cselect_b64 vcc, -1, 0
	s_and_b64 s[80:81], s[80:81], vcc
	s_andn2_b64 vcc, exec, s[80:81]
	s_cbranch_vccnz .LBB0_611
	s_cmp_gt_i32 s6, s35
	s_cselect_b64 s[6:7], -1, 0
	s_cmp_le_i32 s62, s25
	s_cselect_b64 s[80:81], -1, 0
	s_lshl_b32 s14, s39, 13
	v_add_u32_e32 v82, s14, v160
	ds_read_b128 v[192:195], v82
	ds_read_b128 v[196:199], v82 offset:512
	ds_read_b128 v[200:203], v82 offset:2048
	ds_read_b128 v[204:207], v82 offset:2560
	ds_read_b128 v[208:211], v82 offset:4096
	ds_read_b128 v[212:215], v82 offset:4608
	ds_read_b128 v[216:219], v82 offset:6144
	ds_read_b128 v[220:223], v82 offset:6656
	v_sub_f32_e32 v34, v187, v188
	v_mov_b32_e32 v35, v34
	v_mov_b32_e32 v36, v34
	v_mov_b32_e32 v37, v34
	v_mov_b32_e32 v38, v34
	v_mov_b32_e32 v39, v34
	v_mov_b32_e32 v40, v34
	v_mov_b32_e32 v41, v34
	v_mov_b32_e32 v42, v34
	v_mov_b32_e32 v43, v34
	v_mov_b32_e32 v44, v34
	v_mov_b32_e32 v45, v34
	v_mov_b32_e32 v46, v34
	v_mov_b32_e32 v47, v34
	v_mov_b32_e32 v48, v34
	v_mov_b32_e32 v49, v34
	s_sub_i32 s11, s62, s66
	s_or_b64 s[6:7], s[6:7], s[80:81]
	s_waitcnt lgkmcnt(6)
	v_mfma_f32_32x32x16_bf16 v[50:65], v[192:195], v[66:69], v[34:49]
	s_andn2_b64 vcc, exec, s[6:7]
	v_mfma_f32_32x32x16_bf16 v[34:49], v[196:199], v[66:69], v[34:49]
	s_waitcnt lgkmcnt(4)
	v_mfma_f32_32x32x16_bf16 v[50:65], v[200:203], v[70:73], v[50:65]
	v_mfma_f32_32x32x16_bf16 v[34:49], v[204:207], v[70:73], v[34:49]
	s_waitcnt lgkmcnt(2)
	v_mfma_f32_32x32x16_bf16 v[50:65], v[208:211], v[74:77], v[50:65]
	v_mfma_f32_32x32x16_bf16 v[34:49], v[212:215], v[74:77], v[34:49]
	v_lshl_add_u32 v82, s11, 2, v164
	s_waitcnt lgkmcnt(0)
	v_mfma_f32_32x32x16_bf16 v[50:65], v[216:219], v[78:81], v[50:65]
	v_mfma_f32_32x32x16_bf16 v[34:49], v[220:223], v[78:81], v[34:49]
	ds_read_b128 v[192:195], v82 offset:640
	ds_read_b128 v[196:199], v82 offset:512
	ds_read_b128 v[200:203], v82 offset:544
	ds_read_b128 v[204:207], v82 offset:672
	ds_read_b128 v[208:211], v82 offset:576
	ds_read_b128 v[212:215], v82 offset:704
	ds_read_b128 v[216:219], v82 offset:608
	ds_read_b128 v[220:223], v82 offset:736
	s_waitcnt lgkmcnt(0)
	s_nop 1
	v_sub_f32_e32 v57, v57, v203
	v_sub_f32_e32 v61, v61, v211
	v_sub_f32_e32 v60, v60, v210
	v_sub_f32_e32 v65, v65, v219
	v_sub_f32_e32 v64, v64, v218
	v_sub_f32_e32 v63, v63, v217
	v_sub_f32_e32 v62, v62, v216
	v_sub_f32_e32 v59, v59, v209
	v_sub_f32_e32 v58, v58, v208
	v_sub_f32_e32 v56, v56, v202
	v_sub_f32_e32 v55, v55, v201
	v_sub_f32_e32 v54, v54, v200
	v_sub_f32_e32 v53, v53, v199
	v_sub_f32_e32 v52, v52, v198
	v_sub_f32_e32 v51, v51, v197
	v_sub_f32_e32 v50, v50, v196
	v_sub_f32_e32 v49, v49, v223
	v_sub_f32_e32 v48, v48, v222
	v_sub_f32_e32 v47, v47, v221
	v_sub_f32_e32 v46, v46, v220
	v_sub_f32_e32 v45, v45, v215
	v_sub_f32_e32 v44, v44, v214
	v_sub_f32_e32 v43, v43, v213
	v_sub_f32_e32 v42, v42, v212
	v_sub_f32_e32 v41, v41, v207
	v_sub_f32_e32 v40, v40, v206
	v_sub_f32_e32 v39, v39, v205
	v_sub_f32_e32 v38, v38, v204
	v_sub_f32_e32 v37, v37, v195
	v_sub_f32_e32 v36, v36, v194
	v_sub_f32_e32 v35, v35, v193
	v_sub_f32_e32 v34, v34, v192
	s_cbranch_vccnz .LBB0_606
; template <int D, bool MASK, bool BIAS, bool SINK, bool REV, bool O8, class BG>
; __device__ __forceinline__ void attn_unit(const Prm& P, LAS unsigned char* lds, BG& bg) {
;     ...
;             if (MASK && need_mask) {
;                 const int dq = qpos - kbase; int lo = dq - P.window + 1; lo = lo > -kbase ? lo : -kbase;
;                 const int lo2 = lo - 4 * hi, hi2 = dq - 4 * hi;
; #pragma unroll
;                 for (int r = 0; r < 16; ++r) {
;                     const int kr = (r & 3) + 8 * (r >> 2);
;                     if (!(kr >= lo2 && kr <= hi2)) p0[r] = -INFINITY;
;                     if (!(kr + 32 >= lo2 && kr + 32 <= hi2)) p1[r] = -INFINITY;
;                 }
	v_subrev_u32_e32 v82, s62, v89
	v_add_u32_e32 v91, 0xffffff81, v82
	s_sub_i32 s6, 0, s62
	v_max_i32_e32 v91, s6, v91
	v_sub_u32_e32 v91, v91, v161
	v_sub_u32_e32 v82, v82, v161
	v_cmp_lt_i32_e32 vcc, 0, v91
	v_cmp_gt_i32_e64 s[6:7], 0, v82
	s_or_b64 vcc, vcc, s[6:7]
	v_cndmask_b32_e32 v50, v50, v184, vcc
	v_cmp_lt_i32_e32 vcc, 32, v91
	v_cmp_gt_i32_e64 s[6:7], 32, v82
	s_or_b64 vcc, vcc, s[6:7]
	v_cndmask_b32_e32 v34, v34, v184, vcc
	v_cmp_lt_i32_e32 vcc, 1, v91
	v_cmp_gt_i32_e64 s[6:7], 1, v82
	s_or_b64 vcc, vcc, s[6:7]
	v_cndmask_b32_e32 v51, v51, v184, vcc
	v_cmp_lt_i32_e32 vcc, 33, v91
	v_cmp_gt_i32_e64 s[6:7], 33, v82
	s_or_b64 vcc, vcc, s[6:7]
	v_cndmask_b32_e32 v35, v35, v184, vcc
	v_cmp_lt_i32_e32 vcc, 2, v91
	v_cmp_gt_i32_e64 s[6:7], 2, v82
	s_or_b64 vcc, vcc, s[6:7]
	v_cndmask_b32_e32 v52, v52, v184, vcc
	v_cmp_lt_i32_e32 vcc, 34, v91
	v_cmp_gt_i32_e64 s[6:7], 34, v82
	s_or_b64 vcc, vcc, s[6:7]
	v_cndmask_b32_e32 v36, v36, v184, vcc
	v_cmp_lt_i32_e32 vcc, 3, v91
	v_cmp_gt_i32_e64 s[6:7], 3, v82
	s_or_b64 vcc, vcc, s[6:7]
	v_cndmask_b32_e32 v53, v53, v184, vcc
	v_cmp_lt_i32_e32 vcc, 35, v91
	v_cmp_gt_i32_e64 s[6:7], 35, v82
	s_or_b64 vcc, vcc, s[6:7]
	v_cndmask_b32_e32 v37, v37, v184, vcc
	v_cmp_lt_i32_e32 vcc, 8, v91
	v_cmp_gt_i32_e64 s[6:7], 8, v82
	s_or_b64 vcc, vcc, s[6:7]
	v_cndmask_b32_e32 v54, v54, v184, vcc
	v_cmp_lt_i32_e32 vcc, 40, v91
	v_cmp_gt_i32_e64 s[6:7], 40, v82
	s_or_b64 vcc, vcc, s[6:7]
	v_cndmask_b32_e32 v38, v38, v184, vcc
	v_cmp_lt_i32_e32 vcc, 9, v91
	v_cmp_gt_i32_e64 s[6:7], 9, v82
	s_or_b64 vcc, vcc, s[6:7]
	v_cndmask_b32_e32 v55, v55, v184, vcc
	v_cmp_lt_i32_e32 vcc, 41, v91
	v_cmp_gt_i32_e64 s[6:7], 41, v82
	s_or_b64 vcc, vcc, s[6:7]
	v_cndmask_b32_e32 v39, v39, v184, vcc
	v_cmp_lt_i32_e32 vcc, 10, v91
	v_cmp_gt_i32_e64 s[6:7], 10, v82
	s_or_b64 vcc, vcc, s[6:7]
	v_cndmask_b32_e32 v56, v56, v184, vcc
	v_cmp_lt_i32_e32 vcc, 42, v91
	v_cmp_gt_i32_e64 s[6:7], 42, v82
	s_or_b64 vcc, vcc, s[6:7]
	v_cndmask_b32_e32 v40, v40, v184, vcc
	v_cmp_lt_i32_e32 vcc, 11, v91
	v_cmp_gt_i32_e64 s[6:7], 11, v82
	s_or_b64 vcc, vcc, s[6:7]
	v_cndmask_b32_e32 v57, v57, v184, vcc
	v_cmp_lt_i32_e32 vcc, 43, v91
	v_cmp_gt_i32_e64 s[6:7], 43, v82
	s_or_b64 vcc, vcc, s[6:7]
	v_cndmask_b32_e32 v41, v41, v184, vcc
	v_cmp_lt_i32_e32 vcc, 16, v91
	v_cmp_gt_i32_e64 s[6:7], 16, v82
	s_or_b64 vcc, vcc, s[6:7]
	v_cndmask_b32_e32 v58, v58, v184, vcc
	v_cmp_lt_i32_e32 vcc, 48, v91
	v_cmp_gt_i32_e64 s[6:7], 48, v82
	s_or_b64 vcc, vcc, s[6:7]
	v_cndmask_b32_e32 v42, v42, v184, vcc
	v_cmp_lt_i32_e32 vcc, 17, v91
	v_cmp_gt_i32_e64 s[6:7], 17, v82
	s_or_b64 vcc, vcc, s[6:7]
	v_cndmask_b32_e32 v59, v59, v184, vcc
	v_cmp_lt_i32_e32 vcc, 49, v91
	v_cmp_gt_i32_e64 s[6:7], 49, v82
	s_or_b64 vcc, vcc, s[6:7]
	v_cndmask_b32_e32 v43, v43, v184, vcc
	v_cmp_lt_i32_e32 vcc, 18, v91
	v_cmp_gt_i32_e64 s[6:7], 18, v82
	s_or_b64 vcc, vcc, s[6:7]
	v_cndmask_b32_e32 v60, v60, v184, vcc
	v_cmp_lt_i32_e32 vcc, 50, v91
	v_cmp_gt_i32_e64 s[6:7], 50, v82
	s_or_b64 vcc, vcc, s[6:7]
	v_cndmask_b32_e32 v44, v44, v184, vcc
	v_cmp_lt_i32_e32 vcc, 19, v91
	v_cmp_gt_i32_e64 s[6:7], 19, v82
	s_or_b64 vcc, vcc, s[6:7]
	v_cndmask_b32_e32 v61, v61, v184, vcc
	v_cmp_lt_i32_e32 vcc, 51, v91
	v_cmp_gt_i32_e64 s[6:7], 51, v82
	s_or_b64 vcc, vcc, s[6:7]
	v_cndmask_b32_e32 v45, v45, v184, vcc
	v_cmp_lt_i32_e32 vcc, 24, v91
	v_cmp_gt_i32_e64 s[6:7], 24, v82
	s_or_b64 vcc, vcc, s[6:7]
	v_cndmask_b32_e32 v62, v62, v184, vcc
	v_cmp_lt_i32_e32 vcc, 56, v91
	v_cmp_gt_i32_e64 s[6:7], 56, v82
	s_or_b64 vcc, vcc, s[6:7]
	v_cndmask_b32_e32 v46, v46, v184, vcc
	v_cmp_lt_i32_e32 vcc, 25, v91
	v_cmp_gt_i32_e64 s[6:7], 25, v82
	s_or_b64 vcc, vcc, s[6:7]
	v_cndmask_b32_e32 v63, v63, v184, vcc
	v_cmp_lt_i32_e32 vcc, 57, v91
	v_cmp_gt_i32_e64 s[6:7], 57, v82
	s_or_b64 vcc, vcc, s[6:7]
	v_cndmask_b32_e32 v47, v47, v184, vcc
	v_cmp_lt_i32_e32 vcc, 26, v91
	v_cmp_gt_i32_e64 s[6:7], 26, v82
	s_or_b64 vcc, vcc, s[6:7]
	v_cndmask_b32_e32 v64, v64, v184, vcc
	v_cmp_lt_i32_e32 vcc, 58, v91
	v_cmp_gt_i32_e64 s[6:7], 58, v82
	s_or_b64 vcc, vcc, s[6:7]
	v_cndmask_b32_e32 v48, v48, v184, vcc
	v_cmp_lt_i32_e32 vcc, 27, v91
	v_cmp_gt_i32_e64 s[6:7], 27, v82
	s_or_b64 vcc, vcc, s[6:7]
	v_cndmask_b32_e32 v65, v65, v184, vcc
	v_cmp_lt_i32_e32 vcc, 59, v91
	v_cmp_gt_i32_e64 s[6:7], 59, v82
	s_or_b64 vcc, vcc, s[6:7]
	v_cndmask_b32_e32 v49, v49, v184, vcc
